# HGRN2 chunk loop: also hoist the conditional fourth prefix read to issue with the other two after the first barrier; waves 0-1 re-enter the state update past the MFMA-hazard nops
# baseline (speedup 1.0000x reference)
.Lhg_295x:
	v_pk_mul_f32 v[4:5], v[4:5], v[60:61]
	s_waitcnt lgkmcnt(4)
	v_pk_mul_f32 v[8:9], v[8:9], v[56:57]
	s_waitcnt lgkmcnt(2)
	v_pk_mul_f32 v[12:13], v[12:13], v[52:53]
	s_waitcnt lgkmcnt(0)
	v_pk_mul_f32 v[16:17], v[16:17], v[64:65]
	v_pk_mul_f32 v[2:3], v[2:3], v[58:59]
	v_pk_mul_f32 v[6:7], v[6:7], v[54:55]
	v_pk_mul_f32 v[10:11], v[10:11], v[50:51]
	v_pk_mul_f32 v[14:15], v[14:15], v[62:63]
	v_pk_fma_f32 v[98:99], v[98:99], v[48:49], v[16:17]
	v_pk_fma_f32 v[96:97], v[96:97], v[46:47], v[14:15]
	v_pk_fma_f32 v[94:95], v[94:95], v[44:45], v[12:13]
	v_pk_fma_f32 v[92:93], v[92:93], v[42:43], v[10:11]
	v_pk_fma_f32 v[90:91], v[90:91], v[40:41], v[8:9]
	v_pk_fma_f32 v[88:89], v[88:89], v[38:39], v[6:7]
	v_pk_fma_f32 v[86:87], v[86:87], v[36:37], v[4:5]
	v_pk_fma_f32 v[84:85], v[84:85], v[34:35], v[2:3]
	v_readfirstlane_b32 s98, v0
	s_cmp_lt_u32 s98, 0x80
	s_cbranch_scc1 .Lhg_b1
	s_waitcnt vmcnt(8)
	s_branch .Lhg_bd

.LBB0_298:
	v_lshlrev_b32_e32 v26, 16, v3
	v_sub_f32_e32 v2, 1.0, v26
	v_lshlrev_b32_e32 v24, 16, v12
	v_max_f32_e32 v2, 0x358637bd, v2
	v_sub_f32_e32 v3, 1.0, v24
	v_lshlrev_b32_e32 v22, 16, v13
	v_log_f32_e32 v2, v2
	v_max_f32_e32 v3, 0x358637bd, v3
	v_sub_f32_e32 v12, 1.0, v22
	v_lshlrev_b32_e32 v21, 16, v14
	v_log_f32_e32 v3, v3
	v_max_f32_e32 v12, 0x358637bd, v12
	v_sub_f32_e32 v13, 1.0, v21
	v_log_f32_e32 v12, v12
	v_max_f32_e32 v13, 0x358637bd, v13
	v_log_f32_e32 v13, v13
	v_add_f32_e32 v28, 0, v2
	v_add_f32_e32 v27, v28, v3
	v_add_f32_e32 v25, v27, v12
	v_add_f32_e32 v23, v25, v13
	v_lshlrev_b32_e32 v20, 16, v15
	v_lshlrev_b32_e32 v13, 16, v18
	v_sub_f32_e32 v2, 1.0, v20
	v_lshlrev_b32_e32 v15, 16, v17
	v_sub_f32_e32 v12, 1.0, v13
	v_max_f32_e32 v2, 0x358637bd, v2
	v_sub_f32_e32 v3, 1.0, v15
	v_max_f32_e32 v12, 0x358637bd, v12
	v_log_f32_e32 v2, v2
	v_max_f32_e32 v3, 0x358637bd, v3
	v_log_f32_e32 v14, v12
	v_lshlrev_b32_e32 v12, 16, v19
	v_log_f32_e32 v3, v3
	v_sub_f32_e32 v17, 1.0, v12
	v_max_f32_e32 v17, 0x358637bd, v17
	v_log_f32_e32 v29, v17
	v_add_f32_e32 v19, v23, v2
	v_add_f32_e32 v18, v19, v3
	v_lshlrev_b32_e32 v2, 2, v4
	v_add_f32_e32 v17, v18, v14
	v_add_u32_e32 v3, s25, v2
	v_add_u32_e32 v2, 0, v2
	v_add_f32_e32 v14, v17, v29
	v_add_u32_e32 v30, 0x10600, v2
	ds_write_b32 v3, v14
	s_waitcnt lgkmcnt(0)
	s_barrier
	ds_read2st64_b32 v[2:3], v30 offset1:2
	ds_read_b32 v29, v30 offset:1024
	ds_read_b32 v36, v30 offset:1536
	s_andn2_b64 vcc, exec, s[34:35]
	s_waitcnt lgkmcnt(2)
	v_add_f32_e32 v3, v2, v3
	s_waitcnt lgkmcnt(1)
	v_add_f32_e32 v29, v3, v29
	s_cbranch_vccnz .LBB0_300
	v_lshl_add_u32 v31, v4, 2, 0
	v_exp_f32_e32 v32, v3
	v_add_u32_e32 v33, 0x10400, v31
	v_add_u32_e32 v35, 0x10200, v31
	s_waitcnt lgkmcnt(0)
	v_add_f32_e32 v30, v29, v36
	v_sub_f32_e32 v34, v30, v3
	v_exp_f32_e32 v30, v30
	v_exp_f32_e32 v34, v34
	v_add_u32_e32 v31, 0x10000, v31
	ds_write_b32 v31, v30
	ds_write_b32 v35, v34
	ds_write_b32 v33, v32
